# baseline (speedup 1.0000x reference)
.LBB8_5:
	s_ashr_i32 s28, s7, 3
	v_lshlrev_b32_e32 v2, 9, v178
	s_movk_i32 s7, 0x1e00
	v_and_or_b32 v2, v2, s7, v177
	v_lshlrev_b32_e32 v183, 1, v2
	v_mul_lo_u32 v2, s6, v182
	v_add_lshl_u32 v162, v2, v177, 1
	v_lshlrev_b32_e32 v2, 6, v181
	s_movk_i32 s7, 0xc00
	s_lshl_b32 s43, s26, 3
	v_and_or_b32 v184, v2, s7, v176
	v_mul_lo_u32 v2, s6, v180
	s_abs_i32 s44, s43
	v_add_lshl_u32 v164, v2, v177, 1
	v_cvt_f32_u32_e32 v2, s44
	s_sub_i32 s29, 0, s44
	s_add_i32 s27, s27, s28
	s_ashr_i32 s28, s27, 31
	v_rcp_iflag_f32_e32 v2, v2
	s_bfe_i32 s46, s26, 0x1001c
	s_xor_b32 s26, s28, s46
	s_abs_i32 s28, s27
	v_mul_f32_e32 v2, 0x4f7ffffe, v2
	v_cvt_u32_f32_e32 v2, v2
	s_lshr_b32 s36, s19, 6
	s_ashr_i32 s7, s6, 31
	s_lshr_b32 s37, s19, 8
	v_readfirstlane_b32 s47, v2
	s_mul_i32 s29, s29, s47
	s_mul_hi_u32 s29, s47, s29
	s_add_i32 s47, s47, s29
	s_mul_hi_u32 s29, s28, s47
	s_mul_i32 s30, s29, s44
	s_sub_i32 s28, s28, s30
	s_lshl_b64 s[22:23], s[6:7], 8
	s_lshl_b64 s[24:25], s[6:7], 9
	s_lshl_b32 s45, s36, 10
	s_add_i32 s30, s29, 1
	s_sub_i32 s31, s28, s44
	s_cmp_ge_u32 s28, s44
	s_cselect_b32 s29, s30, s29
	s_cselect_b32 s28, s31, s28
	s_add_i32 s30, s29, 1
	s_cmp_ge_u32 s28, s44
	s_cselect_b32 s28, s30, s29
	s_xor_b32 s28, s28, s26
	s_sub_i32 s26, s28, s26
	s_lshl_b32 s28, s26, 3
	s_sub_i32 s29, s33, s28
	s_min_i32 s29, s29, 8
	s_abs_i32 s30, s29
	v_cvt_f32_u32_e32 v2, s30
	s_sub_i32 s34, 0, s30
	s_mul_i32 s26, s26, s43
	v_lshlrev_b32_e32 v3, 6, v179
	v_rcp_iflag_f32_e32 v2, v2
	s_movk_i32 s31, 0x1c00
	s_sub_i32 s26, s27, s26
	v_and_or_b32 v185, v3, s31, v176
	v_mul_f32_e32 v2, 0x4f7ffffe, v2
	v_cvt_u32_f32_e32 v2, v2
	s_abs_i32 s31, s26
	s_xor_b32 s27, s26, s29
	s_ashr_i32 s27, s27, 31
	v_readfirstlane_b32 s35, v2
	s_mul_i32 s34, s34, s35
	s_mul_hi_u32 s34, s35, s34
	s_add_i32 s35, s35, s34
	s_mul_hi_u32 s34, s31, s35
	s_mul_i32 s35, s34, s30
	s_sub_i32 s31, s31, s35
	s_add_i32 s35, s34, 1
	s_sub_i32 s48, s31, s30
	s_cmp_ge_u32 s31, s30
	s_cselect_b32 s34, s35, s34
	s_cselect_b32 s31, s48, s31
	s_add_i32 s35, s34, 1
	s_cmp_ge_u32 s31, s30
	s_cselect_b32 s30, s35, s34
	s_xor_b32 s30, s30, s27
	s_sub_i32 s58, s30, s27
	s_mul_i32 s27, s58, s29
	s_sub_i32 s26, s26, s27
	s_add_i32 s57, s26, s28
	s_ashr_i32 s26, s58, 31
	s_mul_i32 s26, s24, s26
	s_mul_hi_u32 s27, s24, s58
	s_add_i32 s28, s27, s26
	s_lshr_b64 s[26:27], s[6:7], 23
	s_mul_i32 s26, s26, s58
	s_add_i32 s28, s28, s26
	s_mul_i32 s26, s24, s58
	s_waitcnt lgkmcnt(0)
	s_add_u32 s34, s20, s26
	s_addc_u32 s35, s21, s28
	s_lshl_b32 s26, s57, 13
	s_ashr_i32 s27, s26, 31
	s_lshl_b64 s[26:27], s[26:27], 1
	s_add_u32 s28, s8, s26
	s_addc_u32 s29, s9, s27
	s_lshl_b32 s26, s57, 14
	s_ashr_i32 s27, s26, 31
	s_lshl_b64 s[26:27], s[26:27], 1
	s_add_u32 s30, s10, s26
	s_nop 4
	global_load_dwordx4 v[32:35], v184, s[28:29]
	s_addc_u32 s31, s11, s27
	global_load_dwordx4 v[36:39], v185, s[28:29]
	s_add_i32 s52, s45, 0
	global_load_dwordx4 v[40:43], v183, s[30:31]
	s_add_i32 m0, s52, 0x10000
	v_mov_b32_e32 v163, 0
	global_load_lds_dwordx4 v162, s[34:35]
	s_add_i32 m0, s52, 0x12000
	v_mov_b32_e32 v2, v163
	global_load_lds_dwordx4 v164, s[34:35]
	v_mov_b32_e32 v3, v163
	v_mov_b32_e32 v4, v163
	v_mov_b32_e32 v5, v163
	s_add_u32 s26, s28, 0x2000
	v_add_u32_e32 v186, 0, v1
	s_addc_u32 s27, s29, 0
	s_add_u32 s48, s30, 0x4000
	s_addc_u32 s49, s31, 0
	s_nop 4
	global_load_dwordx4 v[52:55], v184, s[26:27]
	global_load_dwordx4 v[56:59], v185, s[26:27]
	s_add_u32 s26, s34, s22
	global_load_dwordx4 v[60:63], v183, s[48:49]
	s_addc_u32 s27, s35, s23
	s_add_i32 m0, s52, 0x14000
	v_mov_b32_e32 v165, v163
	global_load_lds_dwordx4 v162, s[26:27]
	s_add_i32 m0, s52, 0x16000
	s_add_u32 s48, s28, 0x80
	global_load_lds_dwordx4 v164, s[26:27]
	s_addc_u32 s49, s29, 0
	s_nop 4
	global_load_dwordx4 v[72:75], v184, s[48:49]
	v_lshl_add_u64 v[18:19], s[34:35], 0, v[162:163]
	v_lshl_add_u64 v[22:23], s[26:27], 0, v[162:163]
	v_lshl_add_u64 v[24:25], s[26:27], 0, v[164:165]
	s_mov_b64 s[26:27], 0x80
	s_add_u32 s50, s30, 0x80
	global_load_dwordx4 v[76:79], v185, s[48:49]
	v_lshl_add_u64 v[20:21], s[34:35], 0, v[164:165]
	s_addc_u32 s51, s31, 0
	global_load_dwordx4 v[80:83], v183, s[50:51]
	s_add_i32 m0, s52, 0x18000
	v_lshl_add_u64 v[18:19], v[18:19], 0, s[26:27]
	global_load_lds_dwordx4 v[18:19], off
	v_lshl_add_u64 v[18:19], v[20:21], 0, s[26:27]
	s_add_i32 m0, s52, 0x1a000
	s_add_u32 s28, s28, 0x2080
	global_load_lds_dwordx4 v[18:19], off
	s_addc_u32 s29, s29, 0
	s_nop 4
	global_load_dwordx4 v[14:17], v184, s[28:29]
	s_add_u32 s30, s30, 0x4080
	global_load_dwordx4 v[6:9], v185, s[28:29]
	s_addc_u32 s31, s31, 0
	global_load_dwordx4 v[10:13], v183, s[30:31]
	s_add_i32 m0, s52, 0x1c000
	v_lshl_add_u64 v[18:19], v[22:23], 0, s[26:27]
	global_load_lds_dwordx4 v[18:19], off
	v_lshl_add_u64 v[18:19], v[24:25], 0, s[26:27]
	s_add_i32 m0, s52, 0x1e000
	s_load_dword s29, s[0:1], 0x60
	global_load_lds_dwordx4 v[18:19], off
	s_waitcnt vmcnt(7)
	v_pk_add_f16 v32, v32, v40
	v_pk_add_f16 v33, v33, v41
	v_pk_add_f16 v34, v34, v42
	v_pk_add_f16 v35, v35, v43
	v_pk_max_f16 v34, v34, 0
	v_pk_max_f16 v35, v35, 0
	v_pk_max_f16 v33, v33, 0
	v_pk_max_f16 v32, v32, 0
	v_pk_add_f16 v36, v36, v40
	v_pk_add_f16 v37, v37, v41
	v_pk_add_f16 v38, v38, v42
	v_pk_add_f16 v39, v39, v43
	v_pk_max_f16 v39, v39, 0
	v_pk_max_f16 v38, v38, 0
	v_pk_max_f16 v37, v37, 0
	v_pk_max_f16 v36, v36, 0
	ds_write_b128 v186, v[32:35]
	ds_write_b128 v186, v[36:39] offset:8192
	v_pk_add_f16 v52, v52, v60
	v_pk_add_f16 v53, v53, v61
	v_pk_add_f16 v54, v54, v62
	v_pk_add_f16 v55, v55, v63
	v_pk_max_f16 v54, v54, 0
	v_pk_max_f16 v55, v55, 0
	v_pk_max_f16 v53, v53, 0
	v_pk_max_f16 v52, v52, 0
	v_pk_add_f16 v56, v56, v60
	v_pk_add_f16 v57, v57, v61
	v_pk_add_f16 v58, v58, v62
	v_pk_add_f16 v59, v59, v63
	v_pk_max_f16 v58, v58, 0
	v_pk_max_f16 v59, v59, 0
	v_pk_max_f16 v57, v57, 0
	v_pk_max_f16 v56, v56, 0
	ds_write_b128 v186, v[52:55] offset:16384
	ds_write_b128 v186, v[56:59] offset:24576
	v_pk_add_f16 v72, v72, v80
	v_pk_add_f16 v73, v73, v81
	v_pk_add_f16 v74, v74, v82
	v_pk_add_f16 v75, v75, v83
	v_pk_max_f16 v74, v74, 0
	v_pk_max_f16 v75, v75, 0
	v_pk_max_f16 v73, v73, 0
	v_pk_max_f16 v72, v72, 0
	v_pk_add_f16 v76, v76, v80
	v_pk_add_f16 v77, v77, v81
	v_pk_add_f16 v78, v78, v82
	v_pk_add_f16 v79, v79, v83
	v_pk_max_f16 v78, v78, 0
	v_pk_max_f16 v79, v79, 0
	v_pk_max_f16 v77, v77, 0
	v_pk_max_f16 v76, v76, 0
	ds_write_b128 v186, v[72:75] offset:32768
	ds_write_b128 v186, v[76:79] offset:40960
	s_cmp_lg_u32 s37, 1
	s_mov_b32 s48, 0
	s_cbranch_scc1 .LBB8_7
	s_barrier

.LBB8_30:
	v_lshlrev_b32_e32 v2, 10, v178
	s_movk_i32 s5, 0x1c00
	v_and_b32_e32 v0, 8, v178
	v_and_or_b32 v2, v2, s5, v177
	s_movk_i32 s5, 0x70
	s_lshl_b32 s42, s6, 3
	v_and_or_b32 v3, v181, 48, v0
	v_and_or_b32 v0, v179, s5, v0
	s_abs_i32 s43, s42
	v_lshl_or_b32 v170, v0, 7, v176
	v_cvt_f32_u32_e32 v0, s43
	s_add_i32 s4, s7, s4
	s_sub_i32 s7, 0, s43
	s_bfe_i32 s45, s6, 0x1001c
	v_rcp_iflag_f32_e32 v0, v0
	s_abs_i32 s6, s4
	s_lshr_b32 s26, s36, 6
	s_ashr_i32 s19, s18, 31
	v_mul_f32_e32 v0, 0x4f7ffffe, v0
	v_cvt_u32_f32_e32 v0, v0
	s_ashr_i32 s5, s4, 31
	s_lshr_b32 s27, s36, 8
	s_lshl_b64 s[14:15], s[18:19], 8
	v_readfirstlane_b32 s46, v0
	s_mul_i32 s7, s7, s46
	s_mul_hi_u32 s7, s46, s7
	s_add_i32 s46, s46, s7
	s_mul_hi_u32 s7, s6, s46
	s_mul_i32 s20, s7, s43
	s_sub_i32 s6, s6, s20
	s_lshl_b64 s[16:17], s[18:19], 9
	s_lshl_b32 s44, s26, 10
	s_xor_b32 s5, s5, s45
	s_add_i32 s20, s7, 1
	s_sub_i32 s21, s6, s43
	s_cmp_ge_u32 s6, s43
	s_cselect_b32 s7, s20, s7
	s_cselect_b32 s6, s21, s6
	s_add_i32 s20, s7, 1
	s_cmp_ge_u32 s6, s43
	s_cselect_b32 s6, s20, s7
	s_xor_b32 s6, s6, s5
	s_sub_i32 s5, s6, s5
	s_lshl_b32 s6, s5, 3
	s_sub_i32 s7, s33, s6
	s_min_i32 s7, s7, 8
	s_abs_i32 s20, s7
	v_cvt_f32_u32_e32 v0, s20
	s_sub_i32 s24, 0, s20
	s_mul_i32 s5, s5, s42
	s_movk_i32 s21, 0x2000
	v_rcp_iflag_f32_e32 v0, v0
	s_sub_i32 s4, s4, s5
	v_lshlrev_b32_e32 v169, 1, v2
	v_and_or_b32 v2, v175, s21, v2
	v_mul_f32_e32 v0, 0x4f7ffffe, v0
	v_cvt_u32_f32_e32 v0, v0
	s_abs_i32 s21, s4
	s_xor_b32 s5, s4, s7
	s_ashr_i32 s5, s5, 31
	v_readfirstlane_b32 s25, v0
	s_mul_i32 s24, s24, s25
	s_mul_hi_u32 s24, s25, s24
	s_add_i32 s25, s25, s24
	s_mul_hi_u32 s24, s21, s25
	s_mul_i32 s25, s24, s20
	s_sub_i32 s21, s21, s25
	s_add_i32 s25, s24, 1
	s_sub_i32 s28, s21, s20
	s_cmp_ge_u32 s21, s20
	s_cselect_b32 s24, s25, s24
	s_cselect_b32 s21, s28, s21
	s_add_i32 s25, s24, 1
	s_cmp_ge_u32 s21, s20
	s_cselect_b32 s20, s25, s24
	s_xor_b32 s20, s20, s5
	s_sub_i32 s58, s20, s5
	s_mul_i32 s5, s58, s7
	s_sub_i32 s4, s4, s5
	s_add_i32 s57, s4, s6
	s_ashr_i32 s4, s58, 31
	s_mul_i32 s4, s16, s4
	s_mul_hi_u32 s5, s16, s58
	s_add_i32 s6, s5, s4
	s_lshr_b64 s[4:5], s[18:19], 23
	s_mul_i32 s4, s4, s58
	s_add_i32 s6, s6, s4
	s_mul_i32 s4, s16, s58
	s_waitcnt lgkmcnt(0)
	s_add_u32 s24, s12, s4
	s_addc_u32 s25, s13, s6
	s_lshl_b32 s4, s57, 14
	s_ashr_i32 s5, s4, 31
	s_lshl_b64 s[4:5], s[4:5], 1
	s_add_u32 s4, s8, s4
	s_addc_u32 s5, s9, s5
	s_lshl_b32 s6, s57, 15
	v_mul_lo_u32 v4, s18, v182
	v_lshl_or_b32 v168, v3, 7, v176
	v_mul_lo_u32 v3, s18, v180
	s_ashr_i32 s7, s6, 31
	v_add_lshl_u32 v160, v4, v177, 1
	v_add_lshl_u32 v162, v3, v177, 1
	v_lshlrev_b32_e32 v171, 1, v2
	s_lshl_b64 s[6:7], s[6:7], 1
	s_nop 4
	global_load_dwordx4 v[34:37], v168, s[4:5]
	s_add_u32 s6, s10, s6
	global_load_dwordx4 v[38:41], v170, s[4:5]
	s_addc_u32 s7, s11, s7
	global_load_dwordx4 v[42:45], v169, s[6:7]
	s_add_i32 s34, s44, 0
	global_load_dwordx4 v[46:49], v171, s[6:7]
	s_add_i32 m0, s34, 0x10000
	v_add_u32_e32 v175, 0, v1
	global_load_lds_dwordx4 v160, s[24:25]
	s_add_i32 m0, s34, 0x12000
	s_add_u32 s20, s4, 0x4000
	global_load_lds_dwordx4 v162, s[24:25]
	s_addc_u32 s21, s5, 0
	s_add_u32 s28, s6, 0x8000
	s_addc_u32 s29, s7, 0
	s_nop 4
	global_load_dwordx4 v[52:55], v168, s[20:21]
	global_load_dwordx4 v[56:59], v170, s[20:21]
	global_load_dwordx4 v[60:63], v169, s[28:29]
	s_add_u32 s20, s24, s14
	global_load_dwordx4 v[64:67], v171, s[28:29]
	s_addc_u32 s21, s25, s15
	s_add_i32 m0, s34, 0x14000
	v_mov_b32_e32 v161, 0
	global_load_lds_dwordx4 v160, s[20:21]
	s_add_i32 m0, s34, 0x16000
	s_add_u32 s28, s4, 0x80
	global_load_lds_dwordx4 v162, s[20:21]
	s_addc_u32 s29, s5, 0
	s_nop 4
	global_load_dwordx4 v[72:75], v168, s[28:29]
	v_mov_b32_e32 v163, v161
	s_add_u32 s30, s6, 0x80
	global_load_dwordx4 v[76:79], v170, s[28:29]
	v_lshl_add_u64 v[18:19], s[24:25], 0, v[160:161]
	v_lshl_add_u64 v[16:17], s[20:21], 0, v[160:161]
	v_lshl_add_u64 v[22:23], s[20:21], 0, v[162:163]
	s_mov_b64 s[20:21], 0x80
	s_addc_u32 s31, s7, 0
	global_load_dwordx4 v[80:83], v169, s[30:31]
	v_lshl_add_u64 v[20:21], s[24:25], 0, v[162:163]
	global_load_dwordx4 v[84:87], v171, s[30:31]
	s_add_i32 m0, s34, 0x18000
	v_lshl_add_u64 v[18:19], v[18:19], 0, s[20:21]
	global_load_lds_dwordx4 v[18:19], off
	v_lshl_add_u64 v[18:19], v[20:21], 0, s[20:21]
	s_add_i32 m0, s34, 0x1a000
	s_add_u32 s4, s4, 0x4080
	global_load_lds_dwordx4 v[18:19], off
	s_addc_u32 s5, s5, 0
	s_nop 4
	global_load_dwordx4 v[8:11], v168, s[4:5]
	s_add_u32 s6, s6, 0x8080
	global_load_dwordx4 v[0:3], v170, s[4:5]
	s_addc_u32 s7, s7, 0
	global_load_dwordx4 v[12:15], v169, s[6:7]
	global_load_dwordx4 v[4:7], v171, s[6:7]
	s_add_i32 m0, s34, 0x1c000
	v_lshl_add_u64 v[16:17], v[16:17], 0, s[20:21]
	global_load_lds_dwordx4 v[16:17], off
	v_lshl_add_u64 v[16:17], v[22:23], 0, s[20:21]
	s_add_i32 m0, s34, 0x1e000
	s_cmp_lg_u32 s27, 1
	global_load_lds_dwordx4 v[16:17], off
	s_waitcnt vmcnt(8)
	v_pk_add_f16 v32, v34, v42
	v_pk_add_f16 v34, v35, v43
	v_pk_add_f16 v35, v36, v44
	v_pk_add_f16 v36, v37, v45
	v_pk_max_f16 v37, v36, 0
	v_pk_max_f16 v36, v35, 0
	v_pk_max_f16 v35, v34, 0
	v_pk_max_f16 v34, v32, 0
	v_pk_add_f16 v32, v38, v46
	v_pk_add_f16 v38, v39, v47
	v_pk_add_f16 v39, v40, v48
	v_pk_add_f16 v40, v41, v49
	v_pk_max_f16 v41, v40, 0
	v_pk_max_f16 v40, v39, 0
	v_pk_max_f16 v39, v38, 0
	v_pk_max_f16 v38, v32, 0
	ds_write_b128 v175, v[34:37]
	ds_write_b128 v175, v[38:41] offset:8192
	v_pk_add_f16 v52, v52, v60
	v_pk_add_f16 v53, v53, v61
	v_pk_add_f16 v54, v54, v62
	v_pk_add_f16 v55, v55, v63
	v_pk_max_f16 v54, v54, 0
	v_pk_max_f16 v55, v55, 0
	v_pk_max_f16 v53, v53, 0
	v_pk_max_f16 v52, v52, 0
	v_pk_add_f16 v56, v56, v64
	v_pk_add_f16 v57, v57, v65
	v_pk_add_f16 v58, v58, v66
	v_pk_add_f16 v59, v59, v67
	v_pk_max_f16 v58, v58, 0
	v_pk_max_f16 v59, v59, 0
	v_pk_max_f16 v57, v57, 0
	v_pk_max_f16 v56, v56, 0
	ds_write_b128 v175, v[52:55] offset:16384
	ds_write_b128 v175, v[56:59] offset:24576
	v_pk_add_f16 v72, v72, v80
	v_pk_add_f16 v73, v73, v81
	v_pk_add_f16 v74, v74, v82
	v_pk_add_f16 v75, v75, v83
	v_pk_max_f16 v74, v74, 0
	v_pk_max_f16 v75, v75, 0
	v_pk_max_f16 v73, v73, 0
	v_pk_max_f16 v72, v72, 0
	v_pk_add_f16 v76, v76, v84
	v_pk_add_f16 v77, v77, v85
	v_pk_add_f16 v78, v78, v86
	v_pk_add_f16 v79, v79, v87
	v_pk_max_f16 v78, v78, 0
	v_pk_max_f16 v79, v79, 0
	v_pk_max_f16 v77, v77, 0
	v_pk_max_f16 v76, v76, 0
	ds_write_b128 v175, v[72:75] offset:32768
	ds_write_b128 v175, v[76:79] offset:40960
	s_load_dwordx4 s[4:7], s[0:1], 0x68
	s_load_dword s47, s[0:1], 0x78
	s_mov_b32 s48, 0
	s_cbranch_scc1 .LBB8_32
	s_barrier
